# sel: DMA issue uses the scalar-base address form (no per-piece 64-bit VALU add), rescale test branches on vcc directly
# speedup vs baseline: 1.0012x; 1.0012x over previous
; #define LAS __attribute__((address_space(3)))
; __device__ __forceinline__ void ringS_dma(const RingSLane& R, const char* K8p, const char* VTp, LAS unsigned char* sb, int wave) {
;     __builtin_amdgcn_global_load_lds((const unsigned*)(K8p + R.so[0]), (LAS unsigned*)(sb + wave * 1024), 16, 0, 0);
;     __builtin_amdgcn_global_load_lds((const unsigned*)((wave == 0 ? K8p : VTp) + R.so[1]), (LAS unsigned*)(sb + (wave + 8) * 1024), 16, 0, 0);
;     if (wave <= 2) __builtin_amdgcn_global_load_lds((const unsigned*)(VTp + R.so[2]), (LAS unsigned*)(sb + (wave + 16) * 1024), 16, 0, 0);
; }
.Lsel_dodma:
	s_lshr_b32 s12, s60, s36
	s_and_b32 s12, s12, 0xff
	s_lshl_b32 s12, s12, 13
	s_add_u32 s44, s62, s12
	s_addc_u32 s45, s63, 0
	s_add_u32 s12, s64, s12
	s_addc_u32 s13, s65, 0
	s_mul_i32 s97, s37, 0x4c00
	s_add_i32 s97, s98, s97
	s_mov_b32 m0, s97
	s_and_b64 vcc, exec, s[16:17]
	global_load_lds_dwordx4 v102, s[44:45]
	s_cselect_b32 s45, s45, s13
	s_cselect_b32 s44, s44, s12
	s_add_i32 m0, s97, 0x2000
	s_and_b64 vcc, exec, s[10:11]
	global_load_lds_dwordx4 v106, s[44:45]
	s_cbranch_vccnz .Lsel_nodma
	s_add_i32 m0, s97, 0x4000
	s_nop 0
	global_load_lds_dwordx4 v108, s[12:13]

; template <class G> __device__ __forceinline__ void online_sm8(f32x4 (&s)[4], G& g, const float ref) {
;     float mx = s[0][0];
; #pragma unroll
;     for (int T_ = 0; T_ < 4; ++T_)
; #pragma unroll
;         for (int i = 0; i < 4; ++i) mx = fmaxf(mx, s[T_][i]);
;     const float t = mx + (ref - 5.f);
;     if (!__all(t <= g.m + SM_THR8)) {
.LBB0_1806:
	v_max_f32_e32 v18, v84, v85
	v_max3_f32 v18, v18, v86, v87
	v_max3_f32 v18, v18, v88, v89
	v_max3_f32 v18, v18, v90, v91
	v_max3_f32 v18, v18, v92, v93
	v_max3_f32 v18, v18, v94, v95
	v_max3_f32 v18, v18, v96, v97
	v_max3_f32 v114, v18, v98, v99
	v_add_f32_e32 v150, v217, v114
	v_cmp_nle_f32_e32 vcc, v150, v218
	s_cbranch_vccnz .Lsel_resc_g0

; template <class G> __device__ __forceinline__ void online_sm8(f32x4 (&s)[4], G& g, const float ref) {
;     float mx = s[0][0];
; #pragma unroll
;     for (int T_ = 0; T_ < 4; ++T_)
; #pragma unroll
;         for (int i = 0; i < 4; ++i) mx = fmaxf(mx, s[T_][i]);
;     const float t = mx + (ref - 5.f);
;     if (!__all(t <= g.m + SM_THR8)) {
.LBB0_1812:
	v_max_f32_e32 v114, v84, v85
	v_max3_f32 v114, v114, v86, v87
	v_max3_f32 v114, v114, v88, v89
	v_max3_f32 v114, v114, v90, v91
	v_max3_f32 v114, v114, v92, v93
	v_max3_f32 v114, v114, v94, v95
	v_max3_f32 v114, v114, v96, v97
	v_max3_f32 v114, v114, v98, v99
	v_add_f32_e32 v150, v221, v114
	v_cmp_nle_f32_e32 vcc, v150, v222
	s_cbranch_vccnz .Lsel_resc_g1
